# b3 + static conversion queue: layer-0 phase-A converter budget raised from 2 to 4 grabs (less conversion left for layer-0 phase D)
# baseline (speedup 1.0000x reference)
.LBB0_181:
	s_mul_i32 s6, s90, 0xd760
	s_max_i32 s57, s50, s6
	s_sub_i32 s86, s25, s92
	s_and_b64 s[6:7], s[2:3], exec
	s_movk_i32 s4, 0x100
	s_cselect_b32 s6, s4, 0x140
	s_mul_i32 s6, s6, s86
	s_add_i32 s6, s6, s57
	s_min_i32 s50, s6, 0x34920
	s_cmp_lt_i32 s89, 0
	s_mov_b64 s[6:7], -1
	s_cbranch_scc0 .LBB0_712
	s_andn2_b64 vcc, exec, s[2:3]
	s_not_b32 s68, s89
	s_cbranch_vccnz .LBB0_260
	s_add_u32 s26, s52, 0x37200000
	s_addc_u32 s27, s53, 0
	s_add_u32 s28, s52, 0x5200000
	s_addc_u32 s29, s53, 0
	s_waitcnt vmcnt(0)
	v_mov_b32_e32 v1, v0
	s_cmp_gt_u32 s89, 0xffffffdf
	s_cselect_b64 s[6:7], -1, 0
	s_cmp_lt_u32 s89, 0xffffffe0
	v_readfirstlane_b32 s3, v1
	s_cbranch_scc1 .LBB0_185
	s_lshr_b32 s8, s68, 3
	s_and_b32 s2, s68, 7
	s_lshl_b32 s9, s8, 20
	s_add_u32 s18, s26, s9
	s_addc_u32 s19, s27, 0
	s_lshl_b32 s9, s2, 20
	s_add_u32 s20, s28, s9
	s_addc_u32 s21, s29, 0
	s_lshl_b32 s30, s8, 8
	s_lshl_b32 s2, s2, 8
